# n44_outlds_pad10
# speedup vs baseline: 1.0356x; 1.0129x over previous
.LBB2_15:
	v_ashrrev_i32_e32 v163, 31, v162
	v_lshl_or_b32 v164, s30, 4, v132
	v_lshlrev_b64 v[130:131], 11, v[162:163]
	v_mov_b32_e32 v167, 0
	s_waitcnt lgkmcnt(0)
	s_mov_b64 s[50:51], s[0:1]
	v_lshl_add_u64 v[130:131], s[0:1], 0, v[130:131]
	v_lshlrev_b32_e32 v166, 4, v164
	v_lshl_add_u64 v[168:169], v[130:131], 0, v[166:167]
	global_load_dwordx2 v[170:171], v[168:169], off nt
	v_lshlrev_b32_e32 v142, 4, v140
	v_cmp_gt_u32_e64 s[2:3], 16, v140
	v_mov_b32_e32 v140, 0x10000
	v_lshlrev_b32_e32 v130, 8, v139
	v_lshlrev_b32_e32 v131, 4, v132
	v_lshlrev_b32_e32 v132, 3, v138
	v_lshl_or_b32 v177, v138, 14, v142
	v_lshl_or_b32 v139, v139, 11, v140
	v_lshlrev_b32_e32 v140, 10, v138
	v_xor_b32_e32 v138, 1, v138
	v_lshlrev_b32_e32 v141, 12, v1
	v_lshlrev_b32_e32 v138, 10, v138
	v_or3_b32 v179, v139, v138, v142
	v_add_u32_e32 v138, 0x1000, v141
	v_and_b32_e32 v180, 0x3000, v138
	v_add_u32_e32 v138, 0x1400, v141
	v_and_b32_e32 v181, 0x3400, v138
	v_add_u32_e32 v138, 0x1800, v141
	v_and_b32_e32 v182, 0x3800, v138
	v_add_u32_e32 v138, 0x1c00, v141
	v_and_b32_e32 v183, 0x3c00, v138
	s_movk_i32 s4, 0x2000
	v_mov_b32_e32 v138, 0x3000
	v_bitop3_b32 v184, v141, s4, v138 bitop3:0x6c
	v_add_u32_e32 v138, 0x2400, v141
	v_and_b32_e32 v185, 0x3400, v138
	v_add_u32_e32 v138, 0x2800, v141
	v_and_b32_e32 v186, 0x3800, v138
	v_add_u32_e32 v138, 0x2c00, v141
	v_and_b32_e32 v187, 0x3c00, v138
	v_add_u32_e32 v138, 0x3000, v141
	v_and_b32_e32 v188, 0x3000, v138
	v_add_u32_e32 v138, 0x3400, v141
	s_and_b32 s9, s7, 0xffff
	v_cmp_eq_u32_e32 vcc, s14, v133
	v_lshl_or_b32 v131, s16, 10, v131
	s_movk_i32 s0, 0x100
	v_lshlrev_b32_e32 v166, 12, v164
	v_and_b32_e32 v189, 0x3400, v138
	v_add_u32_e32 v138, 0x3800, v141
	s_cmp_lg_u64 vcc, exec
	v_lshl_add_u32 v131, s30, 15, v131
	v_cmp_gt_u32_e64 s[0:1], s0, v0
	v_lshl_add_u64 v[0:1], s[12:13], 0, v[166:167]
	v_and_b32_e32 v190, 0x3800, v138
	v_add_u32_e32 v138, 0x3c00, v141
	v_mov_b32_e32 v172, -1
	s_mov_b32 s11, 0x20000
	s_mov_b32 s10, 0x200400
	s_mov_b32 s8, s6
	s_cselect_b64 s[14:15], -1, 0
	v_or3_b32 v165, v131, v132, v130
	s_mov_b32 s17, 0
	v_cndmask_b32_e64 v133, 0, v137, s[0:1]
	v_cndmask_b32_e64 v132, 0, v136, s[0:1]
	v_cndmask_b32_e64 v131, 0, v135, s[0:1]
	v_cndmask_b32_e64 v130, 0, v134, s[0:1]
	v_cndmask_b32_e64 v137, v137, 0, s[0:1]
	v_cndmask_b32_e64 v136, v136, 0, s[0:1]
	v_cndmask_b32_e64 v135, v135, 0, s[0:1]
	v_cndmask_b32_e64 v134, v134, 0, s[0:1]
	v_or_b32_e32 v176, v141, v142
	v_lshl_add_u64 v[0:1], v[162:163], 2, v[0:1]
	v_or3_b32 v178, v139, v140, v142
	v_and_b32_e32 v191, 0x3c00, v138
	s_mov_b64 s[24:25], 0
	s_mov_b64 s[18:19], 0x400
	s_mov_b64 s[20:21], 0x800
	s_mov_b64 s[22:23], 0xc00
	s_mov_b32 s31, 0x40004000
	v_mov_b32_e32 v173, v172
	v_mov_b32_e32 v192, 0
	v_mov_b32_e32 v193, 0
	s_mov_b32 s33, 0
	v_add_u32_e32 v180, v180, v177
	v_add_u32_e32 v181, v181, v177
	v_add_u32_e32 v182, v182, v177
	v_add_u32_e32 v183, v183, v177
	v_add_u32_e32 v184, v184, v177
	v_add_u32_e32 v185, v185, v177
	v_add_u32_e32 v186, v186, v177
	v_add_u32_e32 v187, v187, v177
	v_add_u32_e32 v188, v188, v177
	v_add_u32_e32 v189, v189, v177
	v_add_u32_e32 v190, v190, v177
	v_add_u32_e32 v191, v191, v177
	v_mov_b32_e32 v166, v176
	v_lshlrev_b32_e32 v242, 12, v164
	v_lshl_add_u32 v242, v162, 2, v242
	v_lshlrev_b32_e32 v243, 11, v162
	v_lshl_add_u32 v243, v164, 4, v243
	v_readfirstlane_b32 s42, v176
	s_or_b32 s42, s42, 0x8000
	s_mov_b32 m0, s42
	s_lshl_b32 s36, s30, 15
	s_add_u32 s54, s6, s36
	s_addc_u32 s55, s7, 0
	s_mov_b64 s[40:41], s[54:55]
	s_mov_b32 s45, 0
	s_mov_b32 s58, 0x40000
	s_mov_b32 s46, 0x180000
	s_mov_b64 s[48:49], s[12:13]
	s_cmp_lg_u64 s[14:15], 0
	s_cselect_b32 s57, 1, 0
	s_cmp_lg_u64 s[0:1], 0
	s_cselect_b32 s59, 1, 0
	s_mov_b32 s47, 0
	s_mov_b32 s60, 0
	s_mov_b32 s44, 0
	s_add_u32 s52, s50, 8
	s_addc_u32 s53, s51, 0
	global_load_dwordx2 v[174:175], v243, s[52:53] nt
	s_add_u32 s52, s50, 0x200000
	s_addc_u32 s53, s51, 0
	s_waitcnt vmcnt(1)
	v_cvt_f32_f16_e32 v250, v170
	v_cvt_f32_f16_sdwa v251, v170 dst_sel:DWORD dst_unused:UNUSED_PAD src0_sel:WORD_1
	v_cvt_f32_f16_e32 v252, v171
	v_cvt_f32_f16_sdwa v253, v171 dst_sel:DWORD dst_unused:UNUSED_PAD src0_sel:WORD_1
	v_pk_add_f32 v[198:199], v[130:131], v[134:135]
	v_pk_add_f32 v[200:201], v[132:133], v[136:137]
	v_mov_b32_e32 v194, 0
	v_mov_b32_e32 v195, 0
	v_mov_b32_e32 v196, 0
	v_mov_b32_e32 v197, 0
	v_pk_add_f32 v[198:199], v[198:199], v[250:251]
	v_pk_add_f32 v[200:201], v[200:201], v[252:253]
	v_lshrrev_b32_e32 v249, 4, v176
	v_and_b32_e32 v248, 15, v249
	v_bfe_u32 v246, v249, 4, 2
	v_lshrrev_b32_e32 v247, 8, v249
	v_and_b32_e32 v245, 3, v247
	v_lshrrev_b32_e32 v244, 2, v247
	v_lshl_add_u32 v246, v244, 2, v246
	v_lshl_add_u32 v246, v245, 3, v246
	v_mul_u32_u24_e32 v244, 33, v248
	v_add_u32_e32 v244, v244, v246
	s_mov_b32 s36, 0x12000
	v_lshl_add_u32 v244, v244, 2, s36
	v_bfe_u32 v246, v249, 5, 1
	v_lshl_add_u32 v246, v247, 1, v246
	v_and_b32_e32 v245, 31, v249
	v_lshl_add_u32 v247, s30, 4, v246
	v_lshlrev_b32_e32 v247, 12, v247
	v_lshrrev_b32_e32 v248, 10, v165
	v_and_b32_e32 v248, 31, v248
	v_lshl_add_u32 v248, v248, 5, v245
	v_lshl_add_u32 v247, v248, 2, v247
	v_mul_u32_u24_e32 v246, 33, v246
	v_add_u32_e32 v246, v246, v245
	v_lshl_add_u32 v246, v246, 2, s36
	s_branch .Lrec_act
	s_nop 0
	s_nop 0
	s_nop 0
	s_nop 0
	s_nop 0
	s_nop 0
	s_nop 0
	s_nop 0
	s_nop 0
	s_nop 0
